# v4: + P4 residual epilogue loads issued 16 deep with counted vmcnt instead of 32 serialised load-wait-store steps
# speedup vs baseline: 1.0116x; 1.0011x over previous
;     __device__ __forceinline__ void operator()(const f32x4 (&acc)[2][2][4][2], const Unit& u, int wr, int wc, int fr, int fq) const {
;         const int row0 = u.pm * BM + wr * 64 + fr, col0 = u.cn * BM + wc * 32 + 4 * fq;
; #pragma unroll
;         for (int ai = 0; ai < 2; ++ai)
; #pragma unroll
;             for (int m = 0; m < 4; ++m) { const size_t off = (size_t)(row0 + ai * HALF + m * 16) * ldc + col0;
; #pragma unroll
;                 for (int bj = 0; bj < 2; ++bj)
; #pragma unroll
;                     for (int n = 0; n < 2; ++n) { const f32x4 b = *(const f32x4*)(base + off + bj * HALF + n * 16); *(f32x4*)(out + off + bj * HALF + n * 16) = acc[ai][bj][m][n] + b; } }
;     }
.LBB0_548:
	v_mov_b32_e32 v2, v0
	s_lshl_b32 s5, s20, 8
	v_readfirstlane_b32 s4, v2
	s_ashr_i32 s11, s4, 2
	s_andn2_b32 s11, s11, 63
	s_lshr_b32 s4, s4, 1
	s_add_i32 s11, s11, s5
	s_lshl_b32 s5, s55, 8
	s_and_b32 s4, s4, 0x60
	v_and_or_b32 v146, v2, 15, s11
	s_or_b32 s4, s4, s5
	v_lshrrev_b32_e32 v2, 2, v2
	v_and_or_b32 v148, v2, 12, s4
	v_ashrrev_i32_e32 v147, 31, v146
	v_ashrrev_i32_e32 v149, 31, v148
	v_lshlrev_b64 v[4:5], 11, v[146:147]
	v_lshl_add_u64 v[4:5], v[4:5], 0, v[148:149]
	v_readlane_b32 s56, v251, 3
	v_lshlrev_b64 v[4:5], 2, v[4:5]
	v_readlane_b32 s57, v251, 4
	v_readlane_b32 s12, v251, 52
	v_readlane_b32 s13, v251, 53
	v_lshl_add_u64 v[150:151], s[56:57], 0, v[4:5]
	v_lshl_add_u64 v[152:153], s[12:13], 0, v[4:5]
	s_mov_b64 s[4:5], 0x100000
	s_and_b64 vcc, exec, s[6:7]
	v_readlane_b32 s58, v251, 5
	v_readlane_b32 s59, v251, 6
	v_readlane_b32 s60, v251, 7
	v_readlane_b32 s61, v251, 8
	v_readlane_b32 s62, v251, 9
	v_readlane_b32 s63, v251, 10
	v_readlane_b32 s64, v251, 11
	v_readlane_b32 s65, v251, 12
	v_readlane_b32 s66, v251, 13
	v_readlane_b32 s67, v251, 14
	v_readlane_b32 s68, v251, 15
	v_readlane_b32 s69, v251, 16
	v_readlane_b32 s70, v251, 17
	v_readlane_b32 s71, v251, 18
	s_add_u32 s98, s56, 0x0
	s_addc_u32 s99, s57, 0
	global_load_dwordx4 v[142:145], v4, s[98:99]
	global_load_dwordx4 v[146:149], v4, s[98:99] offset:64
	global_load_dwordx4 v[150:153], v4, s[98:99] offset:512
	global_load_dwordx4 v[154:157], v4, s[98:99] offset:576
	s_add_u32 s98, s56, 0x20000
	s_addc_u32 s99, s57, 0
	global_load_dwordx4 v[158:161], v4, s[98:99]
	global_load_dwordx4 v[162:165], v4, s[98:99] offset:64
	global_load_dwordx4 v[166:169], v4, s[98:99] offset:512
	global_load_dwordx4 v[170:173], v4, s[98:99] offset:576
	s_add_u32 s98, s56, 0x40000
	s_addc_u32 s99, s57, 0
	global_load_dwordx4 v[174:177], v4, s[98:99]
	global_load_dwordx4 v[178:181], v4, s[98:99] offset:64
	global_load_dwordx4 v[182:185], v4, s[98:99] offset:512
	global_load_dwordx4 v[186:189], v4, s[98:99] offset:576
	s_add_u32 s98, s56, 0x60000
	s_addc_u32 s99, s57, 0
	global_load_dwordx4 v[190:193], v4, s[98:99]
	global_load_dwordx4 v[194:197], v4, s[98:99] offset:64
	global_load_dwordx4 v[198:201], v4, s[98:99] offset:512
	global_load_dwordx4 v[202:205], v4, s[98:99] offset:576
	s_add_u32 s100, s12, 0x0
	s_addc_u32 s101, s13, 0
	s_add_u32 s98, s56, 0x100000
	s_addc_u32 s99, s57, 0
	s_waitcnt vmcnt(15)
	v_pk_add_f32 v[142:143], v[138:139], v[142:143]
	v_pk_add_f32 v[144:145], v[140:141], v[144:145]
	global_store_dwordx4 v4, v[142:145], s[100:101]
	global_load_dwordx4 v[138:141], v4, s[98:99]
	s_waitcnt vmcnt(16)
	v_pk_add_f32 v[146:147], v[134:135], v[146:147]
	v_pk_add_f32 v[148:149], v[136:137], v[148:149]
	global_store_dwordx4 v4, v[146:149], s[100:101] offset:64
	global_load_dwordx4 v[134:137], v4, s[98:99] offset:64
	s_waitcnt vmcnt(17)
	v_pk_add_f32 v[150:151], v[130:131], v[150:151]
	v_pk_add_f32 v[152:153], v[132:133], v[152:153]
	global_store_dwordx4 v4, v[150:153], s[100:101] offset:512
	global_load_dwordx4 v[130:133], v4, s[98:99] offset:512
	s_waitcnt vmcnt(18)
	v_pk_add_f32 v[154:155], v[118:119], v[154:155]
	v_pk_add_f32 v[156:157], v[120:121], v[156:157]
	global_store_dwordx4 v4, v[154:157], s[100:101] offset:576
	global_load_dwordx4 v[118:121], v4, s[98:99] offset:576
	s_add_u32 s100, s12, 0x20000
	s_addc_u32 s101, s13, 0
	s_add_u32 s98, s56, 0x120000
	s_addc_u32 s99, s57, 0
	s_waitcnt vmcnt(19)
	v_pk_add_f32 v[158:159], v[126:127], v[158:159]
	v_pk_add_f32 v[160:161], v[128:129], v[160:161]
	global_store_dwordx4 v4, v[158:161], s[100:101]
	global_load_dwordx4 v[126:129], v4, s[98:99]
	s_waitcnt vmcnt(20)
	v_pk_add_f32 v[162:163], v[122:123], v[162:163]
	v_pk_add_f32 v[164:165], v[124:125], v[164:165]
	global_store_dwordx4 v4, v[162:165], s[100:101] offset:64
	global_load_dwordx4 v[122:125], v4, s[98:99] offset:64
	s_waitcnt vmcnt(21)
	v_pk_add_f32 v[166:167], v[114:115], v[166:167]
	v_pk_add_f32 v[168:169], v[116:117], v[168:169]
	global_store_dwordx4 v4, v[166:169], s[100:101] offset:512
	global_load_dwordx4 v[114:117], v4, s[98:99] offset:512
	s_waitcnt vmcnt(22)
	v_pk_add_f32 v[170:171], v[102:103], v[170:171]
	v_pk_add_f32 v[172:173], v[104:105], v[172:173]
	global_store_dwordx4 v4, v[170:173], s[100:101] offset:576
	global_load_dwordx4 v[102:105], v4, s[98:99] offset:576
	s_add_u32 s100, s12, 0x40000
	s_addc_u32 s101, s13, 0
	s_add_u32 s98, s56, 0x140000
	s_addc_u32 s99, s57, 0
	s_waitcnt vmcnt(23)
	v_pk_add_f32 v[174:175], v[110:111], v[174:175]
	v_pk_add_f32 v[176:177], v[112:113], v[176:177]
	global_store_dwordx4 v4, v[174:177], s[100:101]
	global_load_dwordx4 v[110:113], v4, s[98:99]
	s_waitcnt vmcnt(24)
;     __device__ __forceinline__ void operator()(const f32x4 (&acc)[2][2][4][2], const Unit& u, int wr, int wc, int fr, int fq) const {
;     ...
;             for (int m = 0; m < 4; ++m) { const size_t off = (size_t)(row0 + ai * HALF + m * 16) * ldc + col0;
; #pragma unroll
;                 for (int bj = 0; bj < 2; ++bj)
; #pragma unroll
;                     for (int n = 0; n < 2; ++n) { const f32x4 b = *(const f32x4*)(base + off + bj * HALF + n * 16); *(f32x4*)(out + off + bj * HALF + n * 16) = acc[ai][bj][m][n] + b; } }
	v_pk_add_f32 v[178:179], v[106:107], v[178:179]
	v_pk_add_f32 v[180:181], v[108:109], v[180:181]
	global_store_dwordx4 v4, v[178:181], s[100:101] offset:64
	global_load_dwordx4 v[106:109], v4, s[98:99] offset:64
	s_waitcnt vmcnt(25)
	v_pk_add_f32 v[182:183], v[98:99], v[182:183]
	v_pk_add_f32 v[184:185], v[100:101], v[184:185]
	global_store_dwordx4 v4, v[182:185], s[100:101] offset:512
	global_load_dwordx4 v[98:101], v4, s[98:99] offset:512
	s_waitcnt vmcnt(26)
	v_pk_add_f32 v[186:187], v[86:87], v[186:187]
	v_pk_add_f32 v[188:189], v[88:89], v[188:189]
	global_store_dwordx4 v4, v[186:189], s[100:101] offset:576
	global_load_dwordx4 v[86:89], v4, s[98:99] offset:576
	s_add_u32 s100, s12, 0x60000
	s_addc_u32 s101, s13, 0
	s_add_u32 s98, s56, 0x160000
	s_addc_u32 s99, s57, 0
	s_waitcnt vmcnt(27)
	v_pk_add_f32 v[190:191], v[94:95], v[190:191]
	v_pk_add_f32 v[192:193], v[96:97], v[192:193]
	global_store_dwordx4 v4, v[190:193], s[100:101]
	global_load_dwordx4 v[94:97], v4, s[98:99]
	s_waitcnt vmcnt(28)
	v_pk_add_f32 v[194:195], v[90:91], v[194:195]
	v_pk_add_f32 v[196:197], v[92:93], v[196:197]
	global_store_dwordx4 v4, v[194:197], s[100:101] offset:64
	global_load_dwordx4 v[90:93], v4, s[98:99] offset:64
	s_waitcnt vmcnt(29)
	v_pk_add_f32 v[198:199], v[82:83], v[198:199]
	v_pk_add_f32 v[200:201], v[84:85], v[200:201]
	global_store_dwordx4 v4, v[198:201], s[100:101] offset:512
	global_load_dwordx4 v[82:85], v4, s[98:99] offset:512
	s_waitcnt vmcnt(30)
	v_pk_add_f32 v[202:203], v[78:79], v[202:203]
	v_pk_add_f32 v[204:205], v[80:81], v[204:205]
	global_store_dwordx4 v4, v[202:205], s[100:101] offset:576
	global_load_dwordx4 v[78:81], v4, s[98:99] offset:576
	s_add_u32 s100, s12, 0x100000
	s_addc_u32 s101, s13, 0
	s_waitcnt vmcnt(30)
	v_pk_add_f32 v[138:139], v[74:75], v[138:139]
	v_pk_add_f32 v[140:141], v[76:77], v[140:141]
	global_store_dwordx4 v4, v[138:141], s[100:101]
	s_waitcnt vmcnt(29)
	v_pk_add_f32 v[134:135], v[70:71], v[134:135]
	v_pk_add_f32 v[136:137], v[72:73], v[136:137]
	global_store_dwordx4 v4, v[134:137], s[100:101] offset:64
	s_waitcnt vmcnt(28)
	v_pk_add_f32 v[130:131], v[66:67], v[130:131]
	v_pk_add_f32 v[132:133], v[68:69], v[132:133]
	global_store_dwordx4 v4, v[130:133], s[100:101] offset:512
	s_waitcnt vmcnt(27)
	v_pk_add_f32 v[118:119], v[54:55], v[118:119]
	v_pk_add_f32 v[120:121], v[56:57], v[120:121]
	global_store_dwordx4 v4, v[118:121], s[100:101] offset:576
	s_add_u32 s100, s12, 0x120000
	s_addc_u32 s101, s13, 0
	s_waitcnt vmcnt(26)
	v_pk_add_f32 v[126:127], v[62:63], v[126:127]
	v_pk_add_f32 v[128:129], v[64:65], v[128:129]
	global_store_dwordx4 v4, v[126:129], s[100:101]
	s_waitcnt vmcnt(25)
	v_pk_add_f32 v[122:123], v[58:59], v[122:123]
	v_pk_add_f32 v[124:125], v[60:61], v[124:125]
	global_store_dwordx4 v4, v[122:125], s[100:101] offset:64
	s_waitcnt vmcnt(24)
	v_pk_add_f32 v[114:115], v[50:51], v[114:115]
	v_pk_add_f32 v[116:117], v[52:53], v[116:117]
	global_store_dwordx4 v4, v[114:117], s[100:101] offset:512
	s_waitcnt vmcnt(23)
	v_pk_add_f32 v[102:103], v[38:39], v[102:103]
	v_pk_add_f32 v[104:105], v[40:41], v[104:105]
	global_store_dwordx4 v4, v[102:105], s[100:101] offset:576
	s_add_u32 s100, s12, 0x140000
	s_addc_u32 s101, s13, 0
	s_waitcnt vmcnt(22)
	v_pk_add_f32 v[110:111], v[46:47], v[110:111]
	v_pk_add_f32 v[112:113], v[48:49], v[112:113]
	global_store_dwordx4 v4, v[110:113], s[100:101]
	s_waitcnt vmcnt(21)
	v_pk_add_f32 v[106:107], v[42:43], v[106:107]
	v_pk_add_f32 v[108:109], v[44:45], v[108:109]
	global_store_dwordx4 v4, v[106:109], s[100:101] offset:64
	s_waitcnt vmcnt(20)
	v_pk_add_f32 v[98:99], v[34:35], v[98:99]
	v_pk_add_f32 v[100:101], v[36:37], v[100:101]
	global_store_dwordx4 v4, v[98:101], s[100:101] offset:512
	s_waitcnt vmcnt(19)
	v_pk_add_f32 v[86:87], v[22:23], v[86:87]
	v_pk_add_f32 v[88:89], v[24:25], v[88:89]
	global_store_dwordx4 v4, v[86:89], s[100:101] offset:576
	s_add_u32 s100, s12, 0x160000
	s_addc_u32 s101, s13, 0
	s_waitcnt vmcnt(18)
	v_pk_add_f32 v[94:95], v[30:31], v[94:95]
	v_pk_add_f32 v[96:97], v[32:33], v[96:97]
	global_store_dwordx4 v4, v[94:97], s[100:101]
	s_waitcnt vmcnt(17)
	v_pk_add_f32 v[90:91], v[26:27], v[90:91]
	v_pk_add_f32 v[92:93], v[28:29], v[92:93]
	global_store_dwordx4 v4, v[90:93], s[100:101] offset:64
	s_waitcnt vmcnt(16)
	v_pk_add_f32 v[82:83], v[18:19], v[82:83]
	v_pk_add_f32 v[84:85], v[20:21], v[84:85]
	global_store_dwordx4 v4, v[82:85], s[100:101] offset:512
	s_waitcnt vmcnt(15)
	v_pk_add_f32 v[78:79], v[14:15], v[78:79]
	v_pk_add_f32 v[80:81], v[16:17], v[80:81]
	global_store_dwordx4 v4, v[78:81], s[100:101] offset:576
	s_cbranch_vccnz .LBB0_550
	s_mov_b32 s20, s10
	s_mov_b32 s55, s14
	s_mov_b64 s[4:5], s[18:19]
	s_mov_b64 s[24:25], s[16:17]
	s_branch .LBB0_528

; __global__ void __launch_bounds__(NWAVES * 64, 2) fwd(Args args) {
	.amdhsa_kernel _Z3fwd4Args
		.amdhsa_group_segment_fixed_size 0
		.amdhsa_private_segment_fixed_size 0
		.amdhsa_kernarg_size 400
		.amdhsa_user_sgpr_count 2
		.amdhsa_user_sgpr_dispatch_ptr 0
		.amdhsa_user_sgpr_queue_ptr 0
		.amdhsa_user_sgpr_kernarg_segment_ptr 1
		.amdhsa_user_sgpr_dispatch_id 0
		.amdhsa_user_sgpr_kernarg_preload_length 0
		.amdhsa_user_sgpr_kernarg_preload_offset 0
		.amdhsa_user_sgpr_private_segment_size 0
		.amdhsa_uses_dynamic_stack 0
		.amdhsa_enable_private_segment 0
		.amdhsa_system_sgpr_workgroup_id_x 1
		.amdhsa_system_sgpr_workgroup_id_y 0
		.amdhsa_system_sgpr_workgroup_id_z 0
		.amdhsa_system_sgpr_workgroup_info 0
		.amdhsa_system_vgpr_workitem_id 0
		.amdhsa_next_free_vgpr 252
		.amdhsa_next_free_sgpr 102
		.amdhsa_accum_offset 252
		.amdhsa_reserve_vcc 1
		.amdhsa_float_round_mode_32 0
		.amdhsa_float_round_mode_16_64 0
		.amdhsa_float_denorm_mode_32 3
		.amdhsa_float_denorm_mode_16_64 3
		.amdhsa_dx10_clamp 1
		.amdhsa_ieee_mode 1
		.amdhsa_fp16_overflow 0
		.amdhsa_tg_split 0
		.amdhsa_exception_fp_ieee_invalid_op 0
		.amdhsa_exception_fp_denorm_src 0
		.amdhsa_exception_fp_ieee_div_zero 0
		.amdhsa_exception_fp_ieee_overflow 0
		.amdhsa_exception_fp_ieee_underflow 0
		.amdhsa_exception_fp_ieee_inexact 0
		.amdhsa_exception_int_div_zero 0
	.end_amdhsa_kernel

; __global__ void __launch_bounds__(NWAVES * 64, 2) fwd(Args args) {
amdhsa.kernels:
  - .agpr_count:     0
    .args:
      - .offset:         0
        .size:           144
        .value_kind:     by_value
      - .offset:         144
        .size:           4
        .value_kind:     hidden_block_count_x
      - .offset:         148
        .size:           4
        .value_kind:     hidden_block_count_y
      - .offset:         152
        .size:           4
        .value_kind:     hidden_block_count_z
      - .offset:         156
        .size:           2
        .value_kind:     hidden_group_size_x
      - .offset:         158
        .size:           2
        .value_kind:     hidden_group_size_y
      - .offset:         160
        .size:           2
        .value_kind:     hidden_group_size_z
      - .offset:         162
        .size:           2
        .value_kind:     hidden_remainder_x
      - .offset:         164
        .size:           2
        .value_kind:     hidden_remainder_y
      - .offset:         166
        .size:           2
        .value_kind:     hidden_remainder_z
      - .offset:         184
        .size:           8
        .value_kind:     hidden_global_offset_x
      - .offset:         192
        .size:           8
        .value_kind:     hidden_global_offset_y
      - .offset:         200
        .size:           8
        .value_kind:     hidden_global_offset_z
      - .offset:         208
        .size:           2
        .value_kind:     hidden_grid_dims
      - .offset:         264
        .size:           4
        .value_kind:     hidden_dynamic_lds_size
    .group_segment_fixed_size: 0
    .kernarg_segment_align: 8
    .kernarg_segment_size: 400
    .language:       OpenCL C
    .language_version:
      - 2
      - 0
    .max_flat_workgroup_size: 512
    .name:           _Z3fwd4Args
    .private_segment_fixed_size: 0
    .sgpr_count:     108
    .sgpr_spill_count: 104
    .symbol:         _Z3fwd4Args.kd
    .uniform_work_group_size: 1
    .uses_dynamic_stack: false
    .vgpr_count:     252
    .vgpr_spill_count: 0
    .wavefront_size: 64
